# P2 GEMM unit order: row groups of 16 instead of 8 (fewer distinct operand tiles per XCD round)
# baseline (speedup 1.0000x reference)
.LBB0_192:
	s_add_i32 s5, s18, s10
	s_lshr_b32 s11, s5, 9
	s_lshl_b32 s11, s11, 4
	s_and_b32 s5, s5, 0x1ff
	s_lshr_b32 s20, s5, 4
	s_and_b32 s5, s5, 15
	s_add_i32 s22, s11, s5

.LBB0_212:
	s_ashr_i32 s4, s30, 3
	s_add_i32 s4, s41, s4
	s_lshr_b32 s30, s4, 9
	s_lshl_b32 s30, s30, 4
	s_and_b32 s4, s4, 0x1ff
	s_lshr_b32 s40, s4, 4
	s_and_b32 s4, s4, 15
	s_add_i32 s42, s30, s4
	s_mov_b64 s[44:45], s[18:19]

.LBB0_647:
	s_waitcnt lgkmcnt(0)
	v_lshl_add_u64 v[6:7], s[50:51], 0, v[4:5]
	v_add_co_u32_e32 v10, vcc, 0x46800000, v6
	v_cvt_pk_bf16_f32 v15, v12, v13
	s_nop 0
	v_addc_co_u32_e32 v11, vcc, 0, v7, vcc
	v_add_co_u32_e32 v16, vcc, 0x42800000, v6
	v_lshl_add_u64 v[8:9], s[50:51], 0, v[2:3]
	s_nop 0
	v_addc_co_u32_e32 v17, vcc, 0, v7, vcc
	global_store_dword v[10:11], v15, off
	v_add_co_u32_e32 v10, vcc, 0x600000, v8
	global_load_dword v15, v[16:17], off nt
	s_nop 0
	v_addc_co_u32_e32 v11, vcc, 0, v9, vcc
	global_load_dwordx2 v[16:17], v[10:11], off
	v_add_co_u32_e32 v18, vcc, 0x46810000, v6
	s_add_i32 s48, s48, -16
	s_nop 0
	v_addc_co_u32_e32 v19, vcc, 0, v7, vcc
	v_add_co_u32_e32 v20, vcc, 0x42810000, v6
	v_lshl_add_u64 v[2:3], v[2:3], 0, s[42:43]
	s_nop 0
	v_addc_co_u32_e32 v21, vcc, 0, v7, vcc
	v_add_co_u32_e32 v22, vcc, 0x46820000, v6
	global_load_dword v25, v[20:21], off nt
	s_mov_b64 s[26:27], vcc
	v_add_co_u32_e32 v20, vcc, 0x42820000, v6
	s_mov_b64 s[38:39], vcc
	v_add_co_u32_e32 v24, vcc, 0x46830000, v6
	s_mov_b64 s[34:35], vcc
	v_add_co_u32_e32 v26, vcc, 0x42830000, v6
	s_mov_b64 s[36:37], vcc
	v_add_co_u32_e32 v28, vcc, 0x46840000, v6
	s_mov_b64 s[28:29], vcc
	v_add_co_u32_e32 v30, vcc, 0x42840000, v6
	s_mov_b64 s[30:31], vcc
	v_add_co_u32_e32 v32, vcc, 0x46850000, v6
	s_mov_b64 s[22:23], vcc
	v_add_co_u32_e32 v34, vcc, 0x42850000, v6
	s_mov_b64 s[24:25], vcc
	v_add_co_u32_e32 v36, vcc, 0x46860000, v6
	s_mov_b64 s[18:19], vcc
	v_add_co_u32_e32 v38, vcc, 0x42860000, v6
	s_mov_b64 s[20:21], vcc
	v_add_co_u32_e32 v40, vcc, 0x46870000, v6
	s_mov_b64 s[10:11], vcc
	v_add_co_u32_e32 v42, vcc, 0x42870000, v6
	s_mov_b64 s[12:13], vcc
	v_add_co_u32_e32 v44, vcc, 0x46880000, v6
	s_mov_b64 s[6:7], vcc
	v_add_co_u32_e32 v46, vcc, 0x42880000, v6
	s_mov_b64 s[8:9], vcc
	v_add_co_u32_e32 v8, vcc, 0x601000, v8
	s_mov_b64 s[14:15], vcc
	v_add_co_u32_e32 v48, vcc, 0x46890000, v6
	s_mov_b64 s[16:17], vcc
	v_add_co_u32_e32 v50, vcc, 0x42890000, v6
	v_lshl_add_u64 v[4:5], v[4:5], 0, s[44:45]
	s_nop 0
	v_addc_co_u32_e32 v51, vcc, 0, v7, vcc
	global_load_dword v54, v[50:51], off nt
	v_addc_co_u32_e64 v23, vcc, 0, v7, s[26:27]
	v_addc_co_u32_e64 v21, vcc, 0, v7, s[38:39]
	s_cmp_eq_u32 s48, 0
	s_waitcnt vmcnt(0)
	v_lshlrev_b32_e32 v50, 16, v15
	v_and_b32_e32 v51, 0xffff0000, v15
	v_pk_fma_f32 v[12:13], v[12:13], v[16:17], v[50:51]
	s_nop 0
	v_cvt_pk_bf16_f32 v15, v12, v13
	global_store_dword v[18:19], v15, off
	global_load_dwordx2 v[16:17], v[10:11], off offset:512
	v_add_co_u32_e32 v18, vcc, 0x468a0000, v6
	s_mov_b64 s[26:27], vcc
	v_add_co_u32_e32 v50, vcc, 0x428a0000, v6
	v_lshlrev_b32_e32 v52, 16, v25
	v_and_b32_e32 v53, 0xffff0000, v25
	v_addc_co_u32_e32 v51, vcc, 0, v7, vcc
	global_load_dword v15, v[20:21], off nt
	global_load_dword v55, v[50:51], off nt
	v_addc_co_u32_e64 v25, vcc, 0, v7, s[34:35]
	v_addc_co_u32_e64 v27, vcc, 0, v7, s[36:37]
	v_add_co_u32_e32 v20, vcc, 0x468b0000, v6
	s_mov_b64 s[34:35], vcc
	s_waitcnt vmcnt(2)
	v_pk_fma_f32 v[12:13], v[12:13], v[16:17], v[52:53]
	s_nop 0
	v_cvt_pk_bf16_f32 v16, v12, v13
	global_store_dword v[22:23], v16, off
	global_load_dwordx2 v[16:17], v[10:11], off offset:1024
	v_add_co_u32_e32 v22, vcc, 0x428b0000, v6
	s_waitcnt vmcnt(3)
	v_lshlrev_b32_e32 v50, 16, v15
	v_and_b32_e32 v51, 0xffff0000, v15
	v_addc_co_u32_e32 v23, vcc, 0, v7, vcc
	global_load_dword v15, v[26:27], off nt
	global_load_dword v52, v[22:23], off nt
	v_addc_co_u32_e64 v29, vcc, 0, v7, s[28:29]
	v_addc_co_u32_e64 v31, vcc, 0, v7, s[30:31]
	v_add_co_u32_e32 v22, vcc, 0x468c0000, v6
	s_mov_b64 s[28:29], vcc
	s_waitcnt vmcnt(2)
	v_pk_fma_f32 v[12:13], v[12:13], v[16:17], v[50:51]
	s_nop 0
	v_cvt_pk_bf16_f32 v16, v12, v13
	global_store_dword v[24:25], v16, off
	global_load_dwordx2 v[16:17], v[10:11], off offset:1536
	v_add_co_u32_e32 v24, vcc, 0x428c0000, v6
	s_waitcnt vmcnt(3)
	v_lshlrev_b32_e32 v26, 16, v15
	v_and_b32_e32 v27, 0xffff0000, v15
	v_addc_co_u32_e32 v25, vcc, 0, v7, vcc
	global_load_dword v15, v[30:31], off nt
	global_load_dword v50, v[24:25], off nt
	v_addc_co_u32_e64 v33, vcc, 0, v7, s[22:23]
	v_addc_co_u32_e64 v35, vcc, 0, v7, s[24:25]
	v_add_co_u32_e32 v24, vcc, 0x468d0000, v6
	s_mov_b64 s[22:23], vcc
	s_waitcnt vmcnt(2)
	v_pk_fma_f32 v[12:13], v[12:13], v[16:17], v[26:27]
	s_nop 0
	v_cvt_pk_bf16_f32 v16, v12, v13
	global_store_dword v[28:29], v16, off
	global_load_dwordx2 v[16:17], v[10:11], off offset:2048
	v_add_co_u32_e32 v26, vcc, 0x428d0000, v6
	s_waitcnt vmcnt(3)
	v_lshlrev_b32_e32 v28, 16, v15
	v_and_b32_e32 v29, 0xffff0000, v15
	v_addc_co_u32_e32 v27, vcc, 0, v7, vcc
	global_load_dword v15, v[34:35], off nt
	s_nop 0
	global_load_dword v34, v[26:27], off nt
	v_addc_co_u32_e64 v37, vcc, 0, v7, s[18:19]
	v_addc_co_u32_e64 v39, vcc, 0, v7, s[20:21]
	v_add_co_u32_e32 v26, vcc, 0x468e0000, v6
	s_mov_b64 s[18:19], vcc
	s_waitcnt vmcnt(2)
	v_pk_fma_f32 v[12:13], v[12:13], v[16:17], v[28:29]
	s_nop 0
	v_cvt_pk_bf16_f32 v16, v12, v13
	global_store_dword v[32:33], v16, off
	global_load_dwordx2 v[16:17], v[10:11], off offset:2560
	v_add_co_u32_e32 v28, vcc, 0x428e0000, v6
	s_waitcnt vmcnt(3)
	v_lshlrev_b32_e32 v30, 16, v15
	v_and_b32_e32 v31, 0xffff0000, v15
	v_addc_co_u32_e32 v29, vcc, 0, v7, vcc
	global_load_dword v15, v[38:39], off nt
	global_load_dword v35, v[28:29], off nt
	v_addc_co_u32_e64 v41, vcc, 0, v7, s[10:11]
	v_addc_co_u32_e64 v43, vcc, 0, v7, s[12:13]
	v_add_co_u32_e32 v28, vcc, 0x468f0000, v6
	s_mov_b64 s[10:11], vcc
	s_waitcnt vmcnt(2)
	v_pk_fma_f32 v[12:13], v[12:13], v[16:17], v[30:31]
	s_nop 0
	v_cvt_pk_bf16_f32 v16, v12, v13
	global_store_dword v[36:37], v16, off
	global_load_dwordx2 v[16:17], v[10:11], off offset:3072
	v_add_co_u32_e32 v30, vcc, 0x428f0000, v6
	s_waitcnt vmcnt(3)
	v_lshlrev_b32_e32 v32, 16, v15
	v_and_b32_e32 v33, 0xffff0000, v15
	v_addc_co_u32_e32 v31, vcc, 0, v7, vcc
	global_load_dword v6, v[42:43], off nt
	global_load_dword v15, v[30:31], off nt
	v_addc_co_u32_e64 v45, vcc, 0, v7, s[6:7]
	v_addc_co_u32_e64 v47, vcc, 0, v7, s[8:9]
	v_addc_co_u32_e64 v9, vcc, 0, v9, s[14:15]
	v_addc_co_u32_e64 v49, vcc, 0, v7, s[16:17]
	v_addc_co_u32_e64 v19, vcc, 0, v7, s[26:27]
	v_addc_co_u32_e64 v21, vcc, 0, v7, s[34:35]
	v_addc_co_u32_e64 v23, vcc, 0, v7, s[28:29]
	v_addc_co_u32_e64 v25, vcc, 0, v7, s[22:23]
	v_addc_co_u32_e64 v27, vcc, 0, v7, s[18:19]
	v_addc_co_u32_e64 v29, vcc, 0, v7, s[10:11]
	s_waitcnt vmcnt(4)
	v_and_b32_e32 v7, 0xffff0000, v35
	s_waitcnt vmcnt(2)
	v_pk_fma_f32 v[12:13], v[12:13], v[16:17], v[32:33]
	s_nop 0
	v_cvt_pk_bf16_f32 v16, v12, v13
	global_store_dword v[40:41], v16, off
	global_load_dwordx2 v[10:11], v[10:11], off offset:3584
	s_waitcnt vmcnt(3)
	v_lshlrev_b32_e32 v16, 16, v6
	v_and_b32_e32 v17, 0xffff0000, v6
	global_load_dword v6, v[46:47], off nt
	s_waitcnt vmcnt(1)
	v_pk_fma_f32 v[10:11], v[12:13], v[10:11], v[16:17]
	s_nop 0
	v_cvt_pk_bf16_f32 v12, v10, v11
	global_store_dword v[44:45], v12, off
	global_load_dwordx2 v[12:13], v[8:9], off
	s_waitcnt vmcnt(2)
	v_lshlrev_b32_e32 v16, 16, v6
	v_and_b32_e32 v17, 0xffff0000, v6
	s_waitcnt vmcnt(0)
	v_pk_fma_f32 v[10:11], v[10:11], v[12:13], v[16:17]
	s_nop 0
	v_cvt_pk_bf16_f32 v6, v10, v11
	global_store_dword v[48:49], v6, off
	global_load_dwordx2 v[12:13], v[8:9], off offset:512
	v_lshlrev_b32_e32 v16, 16, v54
	v_and_b32_e32 v17, 0xffff0000, v54
	s_waitcnt vmcnt(0)
	v_pk_fma_f32 v[10:11], v[10:11], v[12:13], v[16:17]
	s_nop 0
	v_cvt_pk_bf16_f32 v6, v10, v11
	global_store_dword v[18:19], v6, off
	global_load_dwordx2 v[12:13], v[8:9], off offset:1024
	v_lshlrev_b32_e32 v16, 16, v55
	v_and_b32_e32 v17, 0xffff0000, v55
	s_waitcnt vmcnt(0)
	v_pk_fma_f32 v[10:11], v[10:11], v[12:13], v[16:17]
	s_nop 0
	v_cvt_pk_bf16_f32 v6, v10, v11
	global_store_dword v[20:21], v6, off
	global_load_dwordx2 v[12:13], v[8:9], off offset:1536
	v_lshlrev_b32_e32 v16, 16, v52
	v_and_b32_e32 v17, 0xffff0000, v52
	s_waitcnt vmcnt(0)
	v_pk_fma_f32 v[10:11], v[10:11], v[12:13], v[16:17]
	s_nop 0
	v_cvt_pk_bf16_f32 v6, v10, v11
	global_store_dword v[22:23], v6, off
	global_load_dwordx2 v[12:13], v[8:9], off offset:2048
	v_lshlrev_b32_e32 v16, 16, v50
	v_and_b32_e32 v17, 0xffff0000, v50
	s_waitcnt vmcnt(0)
	v_pk_fma_f32 v[10:11], v[10:11], v[12:13], v[16:17]
	s_nop 0
	v_cvt_pk_bf16_f32 v6, v10, v11
	global_store_dword v[24:25], v6, off
	global_load_dwordx2 v[12:13], v[8:9], off offset:2560
	v_lshlrev_b32_e32 v16, 16, v34
	v_and_b32_e32 v17, 0xffff0000, v34
	s_waitcnt vmcnt(0)
	v_pk_fma_f32 v[10:11], v[10:11], v[12:13], v[16:17]
	s_nop 0
	v_cvt_pk_bf16_f32 v6, v10, v11
	global_store_dword v[26:27], v6, off
	global_load_dwordx2 v[12:13], v[8:9], off offset:3072
	v_lshlrev_b32_e32 v6, 16, v35
	s_waitcnt vmcnt(0)
	v_pk_fma_f32 v[6:7], v[10:11], v[12:13], v[6:7]
	s_nop 0
	v_cvt_pk_bf16_f32 v10, v6, v7
	global_store_dword v[28:29], v10, off
	global_load_dwordx2 v[8:9], v[8:9], off offset:3584
	v_lshlrev_b32_e32 v10, 16, v15
	v_and_b32_e32 v11, 0xffff0000, v15
	s_waitcnt vmcnt(0)
	v_pk_fma_f32 v[12:13], v[6:7], v[8:9], v[10:11]
	s_cbranch_scc0 .LBB0_647
	v_add_u32_e32 v1, s2, v1
	v_cmp_lt_i32_e32 vcc, s47, v1
	s_or_b64 s[4:5], vcc, s[4:5]
	v_add_u32_e32 v14, s3, v14
	s_andn2_b64 exec, exec, s[4:5]
	s_cbranch_execnz .LBB0_646
